# rotating conversion pipeline (site-3 register fix) + 112 converter workgroups instead of 128
# baseline (speedup 1.0000x reference)
; #define LAS __attribute__((address_space(3)))
; __device__ __forceinline__ void p4_setup(Frame& F) {
;     LAS int* cntl = (LAS int*)(F.lds + PRE_OFF + 2048);
;     cntl[F.tid] = (int)__hip_atomic_load(F.ctl + CW_MCNT + F.tid, RLX_AGENT);
;     __syncthreads();
; }
; __global__ void __launch_bounds__(NWAVES * 64, 2) fwd_kernel(Args args) {
;     ...
;     if (IN(4)) { p4_setup(F);
;         if (((blockIdx.x >> 3) & 1) == 0) {
;             p4_moba_loop(F, A, 0, true); if (F.wave >= 4) conv_wave(F, A); __syncthreads(); }
.LBB0_527:
	s_cmp_gt_i32 s96, 4
	s_cselect_b64 s[0:1], -1, 0
	s_cmp_lt_i32 s97, 5
	s_cselect_b64 s[2:3], -1, 0
	s_or_b64 s[0:1], s[0:1], s[2:3]
	s_and_b64 vcc, exec, s[0:1]
	s_cbranch_vccnz .LBB0_1050
	v_lshlrev_b32_e32 v172, 2, v0
	v_mov_b32_e32 v173, 0
	s_waitcnt lgkmcnt(0)
	v_lshl_add_u64 v[2:3], s[94:95], 0, v[172:173]
	v_add_co_u32_e32 v2, vcc, 0x1000, v2
	s_bfe_u32 s98, s70, 0x40003
	s_cmp_lt_u32 s98, 7
	s_nop 0
	v_addc_co_u32_e32 v3, vcc, 0, v3, vcc
	global_load_dword v1, v[2:3], off sc1
	v_add_u32_e32 v2, 0, v172
	v_add_u32_e32 v2, 0x21800, v2
	s_waitcnt vmcnt(0)
	ds_write_b32 v2, v1
	s_waitcnt lgkmcnt(0)
	s_barrier
	s_cbranch_scc1 .LBB0_530
	v_readlane_b32 s0, v254, 0
	s_and_b32 s6, s0, 0xffffffc0
	v_readlane_b32 s0, v254, 37
	s_lshl_b32 s0, s0, 5
	s_nop 0
	v_writelane_b32 v254, s0, 38
	s_mov_b64 s[0:1], 0
	s_branch .LBB0_531

; __device__ __forceinline__ void cv_load(const float* W, int N, int nblk, int item, int lane, f32x4 (&tv)[16]) {
;     const int kb = item / nblk, nb = item - kb * nblk; const float* p = W + (size_t)(64 * kb + 16 * (lane >> 4)) * N + 64 * nb + 4 * (lane & 15);
; #pragma unroll
;     for (int i = 0; i < 16; ++i) tv[i] = __builtin_nontemporal_load((const f32x4*)(p + (size_t)i * N));
; }
; template <int MODE> __device__ __forceinline__ void cv_run4(const float* W, int K, int N, unsigned char* WT, int item0, int lane) {
;     const int nblk = N / 64; f32x4 ta[16];
; #pragma unroll 1
;     for (int j = 0; j < 4; ++j) { cv_load(W, N, nblk, item0 + j, lane, ta); cv_finish<MODE>(ta, K, nblk, WT, item0 + j, lane); }
.LBB0_979:
	s_lshr_b32 s49, s4, 5
	s_lshl_b32 s50, s49, 11
	v_mov_b32_e32 v3, v69
	v_lshl_or_b32 v2, s49, 6, v1
	s_sub_i32 s49, s47, s50
	s_waitcnt lgkmcnt(1)
	v_subrev_u32_e32 v8, s50, v4
	s_waitcnt lgkmcnt(0)
	v_lshlrev_b64 v[6:7], 13, v[2:3]
	s_add_i32 s50, s48, s49
	v_lshl_add_u64 v[6:7], s[8:9], 0, v[6:7]
	s_ashr_i32 s51, s50, 31
	v_lshl_add_u64 v[6:7], s[50:51], 2, v[6:7]
	v_lshl_add_u64 v[16:17], v[6:7], 0, v[68:69]
	v_add_co_u32_e32 v18, vcc, s17, v16
	v_add_u32_e32 v8, s48, v8
	s_nop 0
	v_addc_co_u32_e32 v19, vcc, 0, v17, vcc
	v_add_co_u32_e32 v20, vcc, s18, v16
	v_ashrrev_i32_e32 v9, 31, v8
	s_nop 0
	v_addc_co_u32_e32 v21, vcc, 0, v17, vcc
	v_add_co_u32_e32 v22, vcc, s19, v16
	v_add_u32_e32 v10, 1, v8
	s_nop 0
	v_addc_co_u32_e32 v23, vcc, 0, v17, vcc
	v_add_co_u32_e32 v24, vcc, s20, v16
	s_waitcnt vmcnt(2)
	v_add_u32_e32 v12, 2, v8
	v_addc_co_u32_e32 v25, vcc, 0, v17, vcc
	v_add_co_u32_e32 v26, vcc, s21, v16
	v_add_u32_e32 v14, 3, v8
	s_nop 0
	v_addc_co_u32_e32 v27, vcc, 0, v17, vcc
	v_add_co_u32_e32 v30, vcc, s22, v16
	v_lshl_add_u64 v[2:3], s[10:11], 0, v[2:3]
	s_nop 0
	v_addc_co_u32_e32 v31, vcc, 0, v17, vcc
	v_add_co_u32_e32 v34, vcc, s23, v16
	v_lshlrev_b64 v[8:9], 11, v[8:9]
	s_nop 0
	v_addc_co_u32_e32 v35, vcc, 0, v17, vcc
	v_add_co_u32_e32 v38, vcc, s24, v16
	v_ashrrev_i32_e32 v11, 31, v10
	s_nop 0
	v_addc_co_u32_e32 v39, vcc, 0, v17, vcc
	v_add_co_u32_e32 v42, vcc, s25, v16
	v_ashrrev_i32_e32 v13, 31, v12
	s_nop 0
	v_addc_co_u32_e32 v43, vcc, 0, v17, vcc
	v_add_co_u32_e32 v46, vcc, s26, v16
	v_ashrrev_i32_e32 v15, 31, v14
	s_nop 0
	v_addc_co_u32_e32 v47, vcc, 0, v17, vcc
	v_add_co_u32_e32 v50, vcc, s27, v16
	v_lshl_add_u64 v[76:77], v[2:3], 0, v[8:9]
	s_nop 0
	v_addc_co_u32_e32 v51, vcc, 0, v17, vcc
	v_add_co_u32_e32 v54, vcc, s28, v16
	v_lshlrev_b64 v[10:11], 11, v[10:11]
	s_nop 0
	v_addc_co_u32_e32 v55, vcc, 0, v17, vcc
	v_add_co_u32_e32 v58, vcc, s29, v16
	v_lshlrev_b64 v[12:13], 11, v[12:13]
	s_nop 0
	v_addc_co_u32_e32 v59, vcc, 0, v17, vcc
	v_add_co_u32_e32 v62, vcc, s30, v16
	v_lshlrev_b64 v[14:15], 11, v[14:15]
	s_nop 0
	v_addc_co_u32_e32 v63, vcc, 0, v17, vcc
	v_add_co_u32_e32 v70, vcc, s31, v16
	global_load_dwordx4 v[6:9], v[16:17], off nt
	s_nop 0
	v_addc_co_u32_e32 v71, vcc, 0, v17, vcc
	v_lshl_add_u64 v[78:79], v[2:3], 0, v[10:11]
	v_lshl_add_u64 v[80:81], v[2:3], 0, v[12:13]
	v_lshl_add_u64 v[2:3], v[2:3], 0, v[14:15]
	global_load_dwordx4 v[10:13], v[18:19], off nt
	global_load_dwordx4 v[14:17], v[20:21], off nt
	s_nop 0
	global_load_dwordx4 v[18:21], v[22:23], off nt
	s_nop 0
	global_load_dwordx4 v[22:25], v[24:25], off nt
	s_nop 0
	global_load_dwordx4 v[26:29], v[26:27], off nt
	s_nop 0
	global_load_dwordx4 v[30:33], v[30:31], off nt
	s_nop 0
	global_load_dwordx4 v[34:37], v[34:35], off nt
	s_nop 0
	global_load_dwordx4 v[38:41], v[38:39], off nt
	s_nop 0
	global_load_dwordx4 v[42:45], v[42:43], off nt
	s_nop 0
	global_load_dwordx4 v[46:49], v[46:47], off nt
	s_nop 0
	global_load_dwordx4 v[50:53], v[50:51], off nt
	s_nop 0
	global_load_dwordx4 v[54:57], v[54:55], off nt
	s_nop 0
	global_load_dwordx4 v[58:61], v[58:59], off nt
	s_nop 0
	global_load_dwordx4 v[62:65], v[62:63], off nt
	s_nop 0
	global_load_dwordx4 v[70:73], v[70:71], off nt
	v_mov_b32_e32 v5, v69
	v_mov_b32_e32 v75, v69
	v_mov_b32_e32 v82, v69
	v_mov_b32_e32 v83, v69
	v_mov_b32_e32 v84, v69
	v_mov_b32_e32 v85, v69
	v_mov_b32_e32 v86, v69
	v_mov_b32_e32 v87, v69
	v_mov_b32_e32 v88, v69
	v_mov_b32_e32 v89, v69
	v_mov_b32_e32 v90, v69
	v_mov_b32_e32 v91, v69
	v_mov_b32_e32 v92, v69
	v_mov_b32_e32 v93, v69
	v_mov_b32_e32 v94, v69
	v_mov_b32_e32 v95, v69
	s_add_i32 s4, s4, 1
	s_add_i32 s48, s48, 64
	s_lshr_b32 s49, s4, 5
	s_lshl_b32 s50, s49, 11
	v_mov_b32_e32 v101, v69
	v_lshl_or_b32 v100, s49, 6, v1
	s_sub_i32 s49, s47, s50
	s_waitcnt lgkmcnt(1)
	v_subrev_u32_e32 v106, s50, v4
	s_waitcnt lgkmcnt(0)
	v_lshlrev_b64 v[104:105], 13, v[100:101]
	s_add_i32 s50, s48, s49
	v_lshl_add_u64 v[104:105], s[8:9], 0, v[104:105]
	s_ashr_i32 s51, s50, 31
	v_lshl_add_u64 v[104:105], s[50:51], 2, v[104:105]
	v_lshl_add_u64 v[114:115], v[104:105], 0, v[68:69]
	v_add_co_u32_e32 v116, vcc, s17, v114
	v_add_u32_e32 v106, s48, v106
	s_nop 0
	v_addc_co_u32_e32 v117, vcc, 0, v115, vcc
	v_add_co_u32_e32 v118, vcc, s18, v114
	v_ashrrev_i32_e32 v107, 31, v106
	s_nop 0
	v_addc_co_u32_e32 v119, vcc, 0, v115, vcc
	v_add_co_u32_e32 v120, vcc, s19, v114
	v_add_u32_e32 v108, 1, v106
	s_nop 0
	v_addc_co_u32_e32 v121, vcc, 0, v115, vcc
	v_add_co_u32_e32 v122, vcc, s20, v114
	s_waitcnt vmcnt(2)
; __device__ __forceinline__ void cv_load(const float* W, int N, int nblk, int item, int lane, f32x4 (&tv)[16]) {
;     const int kb = item / nblk, nb = item - kb * nblk; const float* p = W + (size_t)(64 * kb + 16 * (lane >> 4)) * N + 64 * nb + 4 * (lane & 15);
; #pragma unroll
;     for (int i = 0; i < 16; ++i) tv[i] = __builtin_nontemporal_load((const f32x4*)(p + (size_t)i * N));
; }
; template <int MODE> __device__ __forceinline__ void cv_finish(const f32x4 (&tv)[16], int K, int nblk, unsigned char* WT, int item, int lane) {
;     const int kb = item / nblk, nb = item - kb * nblk, k0 = 64 * kb + 16 * (lane >> 4), n0 = 64 * nb + 4 * (lane & 15);
;     unsigned D[16];
; #pragma unroll
;     for (int i = 0; i < 16; ++i) { const f32x2 a = (f32x2){tv[i].x, tv[i].y} * (f32x2){1024.f, 1024.f}, b = (f32x2){tv[i].z, tv[i].w} * (f32x2){1024.f, 1024.f};
;         D[i] = pk4_fp8(a.x, a.y, b.x, b.y); }
;     unsigned O[4][4];
; #pragma unroll
;     for (int q = 0; q < 4; ++q) { const unsigned a = D[4 * q], b = D[4 * q + 1], c = D[4 * q + 2], d = D[4 * q + 3];
;         const unsigned t0 = __builtin_amdgcn_perm(b, a, 0x05010400u), t1 = __builtin_amdgcn_perm(b, a, 0x07030602u), u0 = __builtin_amdgcn_perm(d, c, 0x05010400u), u1 = __builtin_amdgcn_perm(d, c, 0x07030602u);
;         O[0][q] = __builtin_amdgcn_perm(u0, t0, 0x05040100u); O[1][q] = __builtin_amdgcn_perm(u0, t0, 0x07060302u); O[2][q] = __builtin_amdgcn_perm(u1, t1, 0x05040100u); O[3][q] = __builtin_amdgcn_perm(u1, t1, 0x07060302u); }
; #pragma unroll
;     for (int j = 0; j < 4; ++j) { u32x4 o; o.x = O[j][0]; o.y = O[j][1]; o.z = O[j][2]; o.w = O[j][3];
;         __builtin_nontemporal_store(o, (u32x4*)(WT + (size_t)drow<MODE>(n0 + j) * K + k0)); }
; }
	v_add_u32_e32 v110, 2, v106
	v_addc_co_u32_e32 v123, vcc, 0, v115, vcc
	v_add_co_u32_e32 v124, vcc, s21, v114
	v_add_u32_e32 v112, 3, v106
	s_nop 0
	v_addc_co_u32_e32 v125, vcc, 0, v115, vcc
	v_add_co_u32_e32 v128, vcc, s22, v114
	v_lshl_add_u64 v[100:101], s[10:11], 0, v[100:101]
	s_nop 0
	v_addc_co_u32_e32 v129, vcc, 0, v115, vcc
	v_add_co_u32_e32 v132, vcc, s23, v114
	v_lshlrev_b64 v[106:107], 11, v[106:107]
	s_nop 0
	v_addc_co_u32_e32 v133, vcc, 0, v115, vcc
	v_add_co_u32_e32 v136, vcc, s24, v114
	v_ashrrev_i32_e32 v109, 31, v108
	s_nop 0
	v_addc_co_u32_e32 v137, vcc, 0, v115, vcc
	v_add_co_u32_e32 v140, vcc, s25, v114
	v_ashrrev_i32_e32 v111, 31, v110
	s_nop 0
	v_addc_co_u32_e32 v141, vcc, 0, v115, vcc
	v_add_co_u32_e32 v144, vcc, s26, v114
	v_ashrrev_i32_e32 v113, 31, v112
	s_nop 0
	v_addc_co_u32_e32 v145, vcc, 0, v115, vcc
	v_add_co_u32_e32 v148, vcc, s27, v114
	v_lshl_add_u64 v[172:173], v[100:101], 0, v[106:107]
	s_nop 0
	v_addc_co_u32_e32 v149, vcc, 0, v115, vcc
	v_add_co_u32_e32 v152, vcc, s28, v114
	v_lshlrev_b64 v[108:109], 11, v[108:109]
	s_nop 0
	v_addc_co_u32_e32 v153, vcc, 0, v115, vcc
	v_add_co_u32_e32 v156, vcc, s29, v114
	v_lshlrev_b64 v[110:111], 11, v[110:111]
	s_nop 0
	v_addc_co_u32_e32 v157, vcc, 0, v115, vcc
	v_add_co_u32_e32 v160, vcc, s30, v114
	v_lshlrev_b64 v[112:113], 11, v[112:113]
	s_nop 0
	v_addc_co_u32_e32 v161, vcc, 0, v115, vcc
	v_add_co_u32_e32 v164, vcc, s31, v114
	global_load_dwordx4 v[104:107], v[114:115], off nt
	s_nop 0
	v_addc_co_u32_e32 v165, vcc, 0, v115, vcc
	v_lshl_add_u64 v[174:175], v[100:101], 0, v[108:109]
	v_lshl_add_u64 v[176:177], v[100:101], 0, v[110:111]
	v_lshl_add_u64 v[100:101], v[100:101], 0, v[112:113]
	global_load_dwordx4 v[108:111], v[116:117], off nt
	global_load_dwordx4 v[112:115], v[118:119], off nt
	s_nop 0
	global_load_dwordx4 v[116:119], v[120:121], off nt
	s_nop 0
	global_load_dwordx4 v[120:123], v[122:123], off nt
	s_nop 0
	global_load_dwordx4 v[124:127], v[124:125], off nt
	s_nop 0
	global_load_dwordx4 v[128:131], v[128:129], off nt
	s_nop 0
	global_load_dwordx4 v[132:135], v[132:133], off nt
	s_nop 0
	global_load_dwordx4 v[136:139], v[136:137], off nt
	s_nop 0
	global_load_dwordx4 v[140:143], v[140:141], off nt
	s_nop 0
	global_load_dwordx4 v[144:147], v[144:145], off nt
	s_nop 0
	global_load_dwordx4 v[148:151], v[148:149], off nt
	s_nop 0
	global_load_dwordx4 v[152:155], v[152:153], off nt
	s_nop 0
	global_load_dwordx4 v[156:159], v[156:157], off nt
	s_nop 0
	global_load_dwordx4 v[160:163], v[160:161], off nt
	s_nop 0
	global_load_dwordx4 v[164:167], v[164:165], off nt
	v_mov_b32_e32 v103, v69
	v_mov_b32_e32 v169, v69
	v_mov_b32_e32 v102, v69
	v_mov_b32_e32 v171, v69
	v_mov_b32_e32 v168, v69
	v_mov_b32_e32 v179, v69
	v_mov_b32_e32 v178, v69
	v_mov_b32_e32 v181, v69
	v_mov_b32_e32 v180, v69
	v_mov_b32_e32 v183, v69
	v_mov_b32_e32 v182, v69
	v_mov_b32_e32 v185, v69
	v_mov_b32_e32 v184, v69
	v_mov_b32_e32 v187, v69
	v_mov_b32_e32 v186, v69
	v_mov_b32_e32 v189, v69
	s_add_i32 s4, s4, 1
	s_add_i32 s48, s48, 64
	s_waitcnt vmcnt(31)
	v_pk_mul_f32 v[6:7], v[6:7], s[6:7] op_sel_hi:[1,0]
	s_nop 0
	v_med3_f32 v96, v6, s33, v74
	v_med3_f32 v97, v7, s33, v74
	s_waitcnt vmcnt(30)
	v_pk_mul_f32 v[6:7], v[10:11], s[6:7] op_sel_hi:[1,0]
	s_waitcnt vmcnt(29)
	v_pk_mul_f32 v[10:11], v[14:15], s[6:7] op_sel_hi:[1,0]
	s_waitcnt vmcnt(28)
	v_pk_mul_f32 v[14:15], v[18:19], s[6:7] op_sel_hi:[1,0]
	s_waitcnt vmcnt(27)
	v_pk_mul_f32 v[18:19], v[22:23], s[6:7] op_sel_hi:[1,0]
	s_waitcnt vmcnt(26)
	v_pk_mul_f32 v[22:23], v[26:27], s[6:7] op_sel_hi:[1,0]
	s_waitcnt vmcnt(25)
	v_pk_mul_f32 v[26:27], v[30:31], s[6:7] op_sel_hi:[1,0]
	s_waitcnt vmcnt(24)
	v_pk_mul_f32 v[30:31], v[34:35], s[6:7] op_sel_hi:[1,0]
	s_waitcnt vmcnt(23)
	v_pk_mul_f32 v[34:35], v[38:39], s[6:7] op_sel_hi:[1,0]
	s_waitcnt vmcnt(22)
	v_pk_mul_f32 v[38:39], v[42:43], s[6:7] op_sel_hi:[1,0]
	s_waitcnt vmcnt(21)
	v_pk_mul_f32 v[42:43], v[46:47], s[6:7] op_sel_hi:[1,0]
	s_waitcnt vmcnt(20)
	v_pk_mul_f32 v[46:47], v[50:51], s[6:7] op_sel_hi:[1,0]
	s_waitcnt vmcnt(19)
	v_pk_mul_f32 v[50:51], v[54:55], s[6:7] op_sel_hi:[1,0]
	s_waitcnt vmcnt(18)
	v_pk_mul_f32 v[54:55], v[58:59], s[6:7] op_sel_hi:[1,0]
	s_waitcnt vmcnt(17)
	v_pk_mul_f32 v[58:59], v[62:63], s[6:7] op_sel_hi:[1,0]
	s_waitcnt vmcnt(16)
; __device__ __forceinline__ unsigned pk4_fp8(float a, float b, float c, float d) {
;     a = __builtin_fminf(__builtin_fmaxf(a, -448.f), 448.f); b = __builtin_fminf(__builtin_fmaxf(b, -448.f), 448.f); c = __builtin_fminf(__builtin_fmaxf(c, -448.f), 448.f); d = __builtin_fminf(__builtin_fmaxf(d, -448.f), 448.f);
;     int w = 0; w = __builtin_amdgcn_cvt_pk_fp8_f32(a, b, w, false); w = __builtin_amdgcn_cvt_pk_fp8_f32(c, d, w, true); return (unsigned)w;
; template <int MODE> __device__ __forceinline__ void cv_finish(const f32x4 (&tv)[16], int K, int nblk, unsigned char* WT, int item, int lane) {
;     const int kb = item / nblk, nb = item - kb * nblk, k0 = 64 * kb + 16 * (lane >> 4), n0 = 64 * nb + 4 * (lane & 15);
;     unsigned D[16];
; #pragma unroll
;     for (int i = 0; i < 16; ++i) { const f32x2 a = (f32x2){tv[i].x, tv[i].y} * (f32x2){1024.f, 1024.f}, b = (f32x2){tv[i].z, tv[i].w} * (f32x2){1024.f, 1024.f};
;         D[i] = pk4_fp8(a.x, a.y, b.x, b.y); }
;     unsigned O[4][4];
; #pragma unroll
;     for (int q = 0; q < 4; ++q) { const unsigned a = D[4 * q], b = D[4 * q + 1], c = D[4 * q + 2], d = D[4 * q + 3];
;         const unsigned t0 = __builtin_amdgcn_perm(b, a, 0x05010400u), t1 = __builtin_amdgcn_perm(b, a, 0x07030602u), u0 = __builtin_amdgcn_perm(d, c, 0x05010400u), u1 = __builtin_amdgcn_perm(d, c, 0x07030602u);
;         O[0][q] = __builtin_amdgcn_perm(u0, t0, 0x05040100u); O[1][q] = __builtin_amdgcn_perm(u0, t0, 0x07060302u); O[2][q] = __builtin_amdgcn_perm(u1, t1, 0x05040100u); O[3][q] = __builtin_amdgcn_perm(u1, t1, 0x07060302u); }
; #pragma unroll
;     for (int j = 0; j < 4; ++j) { u32x4 o; o.x = O[j][0]; o.y = O[j][1]; o.z = O[j][2]; o.w = O[j][3];
;         __builtin_nontemporal_store(o, (u32x4*)(WT + (size_t)drow<MODE>(n0 + j) * K + k0)); }
; }
	v_pk_mul_f32 v[62:63], v[70:71], s[6:7] op_sel_hi:[1,0]
	v_med3_f32 v6, v6, s33, v74
	v_med3_f32 v7, v7, s33, v74
	v_med3_f32 v10, v10, s33, v74
	v_med3_f32 v11, v11, s33, v74
	v_med3_f32 v14, v14, s33, v74
	v_med3_f32 v15, v15, s33, v74
	v_med3_f32 v18, v18, s33, v74
	v_med3_f32 v19, v19, s33, v74
	v_med3_f32 v22, v22, s33, v74
	v_med3_f32 v23, v23, s33, v74
	v_med3_f32 v26, v26, s33, v74
	v_med3_f32 v27, v27, s33, v74
	v_med3_f32 v30, v30, s33, v74
	v_med3_f32 v31, v31, s33, v74
	v_med3_f32 v34, v34, s33, v74
	v_med3_f32 v35, v35, s33, v74
	v_med3_f32 v38, v38, s33, v74
	v_med3_f32 v39, v39, s33, v74
	v_med3_f32 v42, v42, s33, v74
	v_med3_f32 v43, v43, s33, v74
	v_med3_f32 v46, v46, s33, v74
	v_med3_f32 v47, v47, s33, v74
	v_med3_f32 v50, v50, s33, v74
	v_med3_f32 v51, v51, s33, v74
	v_med3_f32 v54, v54, s33, v74
	v_med3_f32 v55, v55, s33, v74
	v_med3_f32 v58, v58, s33, v74
	v_med3_f32 v59, v59, s33, v74
	v_med3_f32 v62, v62, s33, v74
	v_med3_f32 v63, v63, s33, v74
	v_cvt_pk_fp8_f32 v5, v96, v97
	v_cvt_pk_fp8_f32 v75, v6, v7
	v_cvt_pk_fp8_f32 v82, v10, v11
	v_cvt_pk_fp8_f32 v83, v14, v15
	v_cvt_pk_fp8_f32 v84, v18, v19
	v_cvt_pk_fp8_f32 v85, v22, v23
	v_cvt_pk_fp8_f32 v86, v26, v27
	v_cvt_pk_fp8_f32 v87, v30, v31
	v_cvt_pk_fp8_f32 v88, v34, v35
	v_cvt_pk_fp8_f32 v89, v38, v39
	v_cvt_pk_fp8_f32 v90, v42, v43
	v_cvt_pk_fp8_f32 v91, v46, v47
	v_cvt_pk_fp8_f32 v92, v50, v51
	v_cvt_pk_fp8_f32 v93, v54, v55
	v_cvt_pk_fp8_f32 v94, v58, v59
	v_cvt_pk_fp8_f32 v95, v62, v63
	v_pk_mul_f32 v[8:9], v[8:9], s[6:7] op_sel_hi:[1,0]
	s_nop 0
	v_med3_f32 v98, v8, s33, v74
	v_med3_f32 v99, v9, s33, v74
	v_pk_mul_f32 v[8:9], v[12:13], s[6:7] op_sel_hi:[1,0]
	v_pk_mul_f32 v[12:13], v[16:17], s[6:7] op_sel_hi:[1,0]
	v_pk_mul_f32 v[16:17], v[20:21], s[6:7] op_sel_hi:[1,0]
	v_pk_mul_f32 v[20:21], v[24:25], s[6:7] op_sel_hi:[1,0]
	v_pk_mul_f32 v[24:25], v[28:29], s[6:7] op_sel_hi:[1,0]
	v_pk_mul_f32 v[28:29], v[32:33], s[6:7] op_sel_hi:[1,0]
	v_pk_mul_f32 v[32:33], v[36:37], s[6:7] op_sel_hi:[1,0]
	v_pk_mul_f32 v[36:37], v[40:41], s[6:7] op_sel_hi:[1,0]
	v_pk_mul_f32 v[40:41], v[44:45], s[6:7] op_sel_hi:[1,0]
	v_pk_mul_f32 v[44:45], v[48:49], s[6:7] op_sel_hi:[1,0]
	v_pk_mul_f32 v[48:49], v[52:53], s[6:7] op_sel_hi:[1,0]
	v_pk_mul_f32 v[52:53], v[56:57], s[6:7] op_sel_hi:[1,0]
	v_pk_mul_f32 v[56:57], v[60:61], s[6:7] op_sel_hi:[1,0]
	v_pk_mul_f32 v[60:61], v[64:65], s[6:7] op_sel_hi:[1,0]
	v_pk_mul_f32 v[64:65], v[72:73], s[6:7] op_sel_hi:[1,0]
	v_med3_f32 v8, v8, s33, v74
	v_med3_f32 v9, v9, s33, v74
	v_med3_f32 v12, v12, s33, v74
	v_med3_f32 v13, v13, s33, v74
	v_med3_f32 v16, v16, s33, v74
	v_med3_f32 v17, v17, s33, v74
	v_med3_f32 v20, v20, s33, v74
	v_med3_f32 v21, v21, s33, v74
	v_med3_f32 v24, v24, s33, v74
	v_med3_f32 v25, v25, s33, v74
	v_med3_f32 v28, v28, s33, v74
	v_med3_f32 v29, v29, s33, v74
	v_med3_f32 v32, v32, s33, v74
	v_med3_f32 v33, v33, s33, v74
	v_med3_f32 v36, v36, s33, v74
	v_med3_f32 v37, v37, s33, v74
	v_med3_f32 v40, v40, s33, v74
	v_med3_f32 v41, v41, s33, v74
	v_med3_f32 v44, v44, s33, v74
	v_med3_f32 v45, v45, s33, v74
	v_med3_f32 v48, v48, s33, v74
	v_med3_f32 v49, v49, s33, v74
	v_med3_f32 v52, v52, s33, v74
	v_med3_f32 v53, v53, s33, v74
	v_med3_f32 v56, v56, s33, v74
	v_med3_f32 v57, v57, s33, v74
	v_med3_f32 v60, v60, s33, v74
	v_med3_f32 v61, v61, s33, v74
	v_med3_f32 v64, v64, s33, v74
	v_med3_f32 v65, v65, s33, v74
	v_cvt_pk_fp8_f32 v5, v98, v99 op_sel:[0,0,1]
	v_cvt_pk_fp8_f32 v75, v8, v9 op_sel:[0,0,1]
	v_cvt_pk_fp8_f32 v82, v12, v13 op_sel:[0,0,1]
	v_cvt_pk_fp8_f32 v83, v16, v17 op_sel:[0,0,1]
	v_cvt_pk_fp8_f32 v84, v20, v21 op_sel:[0,0,1]
	v_cvt_pk_fp8_f32 v85, v24, v25 op_sel:[0,0,1]
	v_cvt_pk_fp8_f32 v86, v28, v29 op_sel:[0,0,1]
	v_cvt_pk_fp8_f32 v87, v32, v33 op_sel:[0,0,1]
	v_cvt_pk_fp8_f32 v88, v36, v37 op_sel:[0,0,1]
	v_cvt_pk_fp8_f32 v89, v40, v41 op_sel:[0,0,1]
	v_cvt_pk_fp8_f32 v90, v44, v45 op_sel:[0,0,1]
	v_cvt_pk_fp8_f32 v91, v48, v49 op_sel:[0,0,1]
	v_cvt_pk_fp8_f32 v92, v52, v53 op_sel:[0,0,1]
	v_cvt_pk_fp8_f32 v93, v56, v57 op_sel:[0,0,1]
	v_cvt_pk_fp8_f32 v94, v60, v61 op_sel:[0,0,1]
	v_cvt_pk_fp8_f32 v95, v64, v65 op_sel:[0,0,1]
	v_perm_b32 v7, v75, v5, s34
	v_perm_b32 v5, v75, v5, s35
	v_perm_b32 v8, v83, v82, s34
	v_perm_b32 v9, v83, v82, s35
	v_perm_b32 v11, v85, v84, s34
	v_perm_b32 v13, v87, v86, s34
	v_perm_b32 v17, v89, v88, s34
	v_perm_b32 v21, v91, v90, s34
	v_perm_b32 v23, v93, v92, s34
	v_perm_b32 v25, v95, v94, s34
	v_perm_b32 v12, v85, v84, s35
	v_perm_b32 v16, v87, v86, s35
	v_perm_b32 v20, v89, v88, s35
	v_perm_b32 v22, v91, v90, s35
	v_perm_b32 v24, v93, v92, s35
	v_perm_b32 v26, v95, v94, s35
	v_perm_b32 v6, v8, v7, s36
	v_perm_b32 v10, v8, v7, s37
	v_perm_b32 v14, v9, v5, s36
	v_perm_b32 v18, v9, v5, s37
	v_perm_b32 v7, v13, v11, s36
	v_perm_b32 v8, v21, v17, s36
	v_perm_b32 v9, v25, v23, s36
	v_perm_b32 v11, v13, v11, s37
	v_perm_b32 v15, v16, v12, s36
	v_perm_b32 v19, v16, v12, s37
	v_perm_b32 v12, v21, v17, s37
	v_perm_b32 v16, v22, v20, s36
	v_perm_b32 v20, v22, v20, s37
	v_perm_b32 v13, v25, v23, s37
	v_perm_b32 v17, v26, v24, s36
	v_perm_b32 v21, v26, v24, s37
	global_store_dwordx4 v[76:77], v[6:9], off nt
	global_store_dwordx4 v[78:79], v[10:13], off nt
	global_store_dwordx4 v[80:81], v[14:17], off nt
	global_store_dwordx4 v[2:3], v[18:21], off nt
	s_lshr_b32 s49, s4, 5
	s_lshl_b32 s50, s49, 11
	v_mov_b32_e32 v3, v69
	v_lshl_or_b32 v2, s49, 6, v1
	s_sub_i32 s49, s47, s50
	s_waitcnt lgkmcnt(1)
	v_subrev_u32_e32 v8, s50, v4
	s_waitcnt lgkmcnt(0)
; __device__ __forceinline__ void cv_load(const float* W, int N, int nblk, int item, int lane, f32x4 (&tv)[16]) {
;     const int kb = item / nblk, nb = item - kb * nblk; const float* p = W + (size_t)(64 * kb + 16 * (lane >> 4)) * N + 64 * nb + 4 * (lane & 15);
; #pragma unroll
;     for (int i = 0; i < 16; ++i) tv[i] = __builtin_nontemporal_load((const f32x4*)(p + (size_t)i * N));
; }
; template <int MODE> __device__ __forceinline__ void cv_finish(const f32x4 (&tv)[16], int K, int nblk, unsigned char* WT, int item, int lane) {
;     const int kb = item / nblk, nb = item - kb * nblk, k0 = 64 * kb + 16 * (lane >> 4), n0 = 64 * nb + 4 * (lane & 15);
;     unsigned D[16];
; #pragma unroll
;     for (int i = 0; i < 16; ++i) { const f32x2 a = (f32x2){tv[i].x, tv[i].y} * (f32x2){1024.f, 1024.f}, b = (f32x2){tv[i].z, tv[i].w} * (f32x2){1024.f, 1024.f};
;         D[i] = pk4_fp8(a.x, a.y, b.x, b.y); }
	v_lshlrev_b64 v[6:7], 13, v[2:3]
	s_add_i32 s50, s48, s49
	v_lshl_add_u64 v[6:7], s[8:9], 0, v[6:7]
	s_ashr_i32 s51, s50, 31
	v_lshl_add_u64 v[6:7], s[50:51], 2, v[6:7]
	v_lshl_add_u64 v[16:17], v[6:7], 0, v[68:69]
	v_add_co_u32_e32 v18, vcc, s17, v16
	v_add_u32_e32 v8, s48, v8
	s_nop 0
	v_addc_co_u32_e32 v19, vcc, 0, v17, vcc
	v_add_co_u32_e32 v20, vcc, s18, v16
	v_ashrrev_i32_e32 v9, 31, v8
	s_nop 0
	v_addc_co_u32_e32 v21, vcc, 0, v17, vcc
	v_add_co_u32_e32 v22, vcc, s19, v16
	v_add_u32_e32 v10, 1, v8
	s_nop 0
	v_addc_co_u32_e32 v23, vcc, 0, v17, vcc
	v_add_co_u32_e32 v24, vcc, s20, v16
	s_waitcnt vmcnt(2)
	v_add_u32_e32 v12, 2, v8
	v_addc_co_u32_e32 v25, vcc, 0, v17, vcc
	v_add_co_u32_e32 v26, vcc, s21, v16
	v_add_u32_e32 v14, 3, v8
	s_nop 0
	v_addc_co_u32_e32 v27, vcc, 0, v17, vcc
	v_add_co_u32_e32 v30, vcc, s22, v16
	v_lshl_add_u64 v[2:3], s[10:11], 0, v[2:3]
	s_nop 0
	v_addc_co_u32_e32 v31, vcc, 0, v17, vcc
	v_add_co_u32_e32 v34, vcc, s23, v16
	v_lshlrev_b64 v[8:9], 11, v[8:9]
	s_nop 0
	v_addc_co_u32_e32 v35, vcc, 0, v17, vcc
	v_add_co_u32_e32 v38, vcc, s24, v16
	v_ashrrev_i32_e32 v11, 31, v10
	s_nop 0
	v_addc_co_u32_e32 v39, vcc, 0, v17, vcc
	v_add_co_u32_e32 v42, vcc, s25, v16
	v_ashrrev_i32_e32 v13, 31, v12
	s_nop 0
	v_addc_co_u32_e32 v43, vcc, 0, v17, vcc
	v_add_co_u32_e32 v46, vcc, s26, v16
	v_ashrrev_i32_e32 v15, 31, v14
	s_nop 0
	v_addc_co_u32_e32 v47, vcc, 0, v17, vcc
	v_add_co_u32_e32 v50, vcc, s27, v16
	v_lshl_add_u64 v[76:77], v[2:3], 0, v[8:9]
	s_nop 0
	v_addc_co_u32_e32 v51, vcc, 0, v17, vcc
	v_add_co_u32_e32 v54, vcc, s28, v16
	v_lshlrev_b64 v[10:11], 11, v[10:11]
	s_nop 0
	v_addc_co_u32_e32 v55, vcc, 0, v17, vcc
	v_add_co_u32_e32 v58, vcc, s29, v16
	v_lshlrev_b64 v[12:13], 11, v[12:13]
	s_nop 0
	v_addc_co_u32_e32 v59, vcc, 0, v17, vcc
	v_add_co_u32_e32 v62, vcc, s30, v16
	v_lshlrev_b64 v[14:15], 11, v[14:15]
	s_nop 0
	v_addc_co_u32_e32 v63, vcc, 0, v17, vcc
	v_add_co_u32_e32 v70, vcc, s31, v16
	global_load_dwordx4 v[6:9], v[16:17], off nt
	s_nop 0
	v_addc_co_u32_e32 v71, vcc, 0, v17, vcc
	v_lshl_add_u64 v[78:79], v[2:3], 0, v[10:11]
	v_lshl_add_u64 v[80:81], v[2:3], 0, v[12:13]
	v_lshl_add_u64 v[2:3], v[2:3], 0, v[14:15]
	global_load_dwordx4 v[10:13], v[18:19], off nt
	global_load_dwordx4 v[14:17], v[20:21], off nt
	s_nop 0
	global_load_dwordx4 v[18:21], v[22:23], off nt
	s_nop 0
	global_load_dwordx4 v[22:25], v[24:25], off nt
	s_nop 0
	global_load_dwordx4 v[26:29], v[26:27], off nt
	s_nop 0
	global_load_dwordx4 v[30:33], v[30:31], off nt
	s_nop 0
	global_load_dwordx4 v[34:37], v[34:35], off nt
	s_nop 0
	global_load_dwordx4 v[38:41], v[38:39], off nt
	s_nop 0
	global_load_dwordx4 v[42:45], v[42:43], off nt
	s_nop 0
	global_load_dwordx4 v[46:49], v[46:47], off nt
	s_nop 0
	global_load_dwordx4 v[50:53], v[50:51], off nt
	s_nop 0
	global_load_dwordx4 v[54:57], v[54:55], off nt
	s_nop 0
	global_load_dwordx4 v[58:61], v[58:59], off nt
	s_nop 0
	global_load_dwordx4 v[62:65], v[62:63], off nt
	s_nop 0
	global_load_dwordx4 v[70:73], v[70:71], off nt
	v_mov_b32_e32 v5, v69
	v_mov_b32_e32 v75, v69
	v_mov_b32_e32 v82, v69
	v_mov_b32_e32 v83, v69
	v_mov_b32_e32 v84, v69
	v_mov_b32_e32 v85, v69
	v_mov_b32_e32 v86, v69
	v_mov_b32_e32 v87, v69
	v_mov_b32_e32 v88, v69
	v_mov_b32_e32 v89, v69
	v_mov_b32_e32 v90, v69
	v_mov_b32_e32 v91, v69
	v_mov_b32_e32 v92, v69
	v_mov_b32_e32 v93, v69
	v_mov_b32_e32 v94, v69
	v_mov_b32_e32 v95, v69
	s_add_i32 s4, s4, 1
	s_add_i32 s48, s48, 64
	s_waitcnt vmcnt(35)
	v_pk_mul_f32 v[104:105], v[104:105], s[6:7] op_sel_hi:[1,0]
	s_nop 0
	v_med3_f32 v188, v104, s33, v74
	v_med3_f32 v191, v105, s33, v74
	s_waitcnt vmcnt(34)
	v_pk_mul_f32 v[104:105], v[108:109], s[6:7] op_sel_hi:[1,0]
	s_waitcnt vmcnt(33)
	v_pk_mul_f32 v[108:109], v[112:113], s[6:7] op_sel_hi:[1,0]
	s_waitcnt vmcnt(32)
	v_pk_mul_f32 v[112:113], v[116:117], s[6:7] op_sel_hi:[1,0]
	s_waitcnt vmcnt(31)
	v_pk_mul_f32 v[116:117], v[120:121], s[6:7] op_sel_hi:[1,0]
	s_waitcnt vmcnt(30)
	v_pk_mul_f32 v[120:121], v[124:125], s[6:7] op_sel_hi:[1,0]
	s_waitcnt vmcnt(29)
	v_pk_mul_f32 v[124:125], v[128:129], s[6:7] op_sel_hi:[1,0]
	s_waitcnt vmcnt(28)
	v_pk_mul_f32 v[128:129], v[132:133], s[6:7] op_sel_hi:[1,0]
	s_waitcnt vmcnt(27)
	v_pk_mul_f32 v[132:133], v[136:137], s[6:7] op_sel_hi:[1,0]
	s_waitcnt vmcnt(26)
	v_pk_mul_f32 v[136:137], v[140:141], s[6:7] op_sel_hi:[1,0]
	s_waitcnt vmcnt(25)
	v_pk_mul_f32 v[140:141], v[144:145], s[6:7] op_sel_hi:[1,0]
	s_waitcnt vmcnt(24)
	v_pk_mul_f32 v[144:145], v[148:149], s[6:7] op_sel_hi:[1,0]
	s_waitcnt vmcnt(23)
	v_pk_mul_f32 v[148:149], v[152:153], s[6:7] op_sel_hi:[1,0]
	s_waitcnt vmcnt(22)
	v_pk_mul_f32 v[152:153], v[156:157], s[6:7] op_sel_hi:[1,0]
	s_waitcnt vmcnt(21)
	v_pk_mul_f32 v[156:157], v[160:161], s[6:7] op_sel_hi:[1,0]
	s_waitcnt vmcnt(20)
; template <int MODE> __device__ __forceinline__ void cv_finish(const f32x4 (&tv)[16], int K, int nblk, unsigned char* WT, int item, int lane) {
;     const int kb = item / nblk, nb = item - kb * nblk, k0 = 64 * kb + 16 * (lane >> 4), n0 = 64 * nb + 4 * (lane & 15);
;     unsigned D[16];
; #pragma unroll
;     for (int i = 0; i < 16; ++i) { const f32x2 a = (f32x2){tv[i].x, tv[i].y} * (f32x2){1024.f, 1024.f}, b = (f32x2){tv[i].z, tv[i].w} * (f32x2){1024.f, 1024.f};
;         D[i] = pk4_fp8(a.x, a.y, b.x, b.y); }
;     unsigned O[4][4];
; #pragma unroll
;     for (int q = 0; q < 4; ++q) { const unsigned a = D[4 * q], b = D[4 * q + 1], c = D[4 * q + 2], d = D[4 * q + 3];
;         const unsigned t0 = __builtin_amdgcn_perm(b, a, 0x05010400u), t1 = __builtin_amdgcn_perm(b, a, 0x07030602u), u0 = __builtin_amdgcn_perm(d, c, 0x05010400u), u1 = __builtin_amdgcn_perm(d, c, 0x07030602u);
;         O[0][q] = __builtin_amdgcn_perm(u0, t0, 0x05040100u); O[1][q] = __builtin_amdgcn_perm(u0, t0, 0x07060302u); O[2][q] = __builtin_amdgcn_perm(u1, t1, 0x05040100u); O[3][q] = __builtin_amdgcn_perm(u1, t1, 0x07060302u); }
; #pragma unroll
;     for (int j = 0; j < 4; ++j) { u32x4 o; o.x = O[j][0]; o.y = O[j][1]; o.z = O[j][2]; o.w = O[j][3];
;         __builtin_nontemporal_store(o, (u32x4*)(WT + (size_t)drow<MODE>(n0 + j) * K + k0)); }
; }
	v_pk_mul_f32 v[160:161], v[164:165], s[6:7] op_sel_hi:[1,0]
	v_med3_f32 v104, v104, s33, v74
	v_med3_f32 v105, v105, s33, v74
	v_med3_f32 v108, v108, s33, v74
	v_med3_f32 v109, v109, s33, v74
	v_med3_f32 v112, v112, s33, v74
	v_med3_f32 v113, v113, s33, v74
	v_med3_f32 v116, v116, s33, v74
	v_med3_f32 v117, v117, s33, v74
	v_med3_f32 v120, v120, s33, v74
	v_med3_f32 v121, v121, s33, v74
	v_med3_f32 v124, v124, s33, v74
	v_med3_f32 v125, v125, s33, v74
	v_med3_f32 v128, v128, s33, v74
	v_med3_f32 v129, v129, s33, v74
	v_med3_f32 v132, v132, s33, v74
	v_med3_f32 v133, v133, s33, v74
	v_med3_f32 v136, v136, s33, v74
	v_med3_f32 v137, v137, s33, v74
	v_med3_f32 v140, v140, s33, v74
	v_med3_f32 v141, v141, s33, v74
	v_med3_f32 v144, v144, s33, v74
	v_med3_f32 v145, v145, s33, v74
	v_med3_f32 v148, v148, s33, v74
	v_med3_f32 v149, v149, s33, v74
	v_med3_f32 v152, v152, s33, v74
	v_med3_f32 v153, v153, s33, v74
	v_med3_f32 v156, v156, s33, v74
	v_med3_f32 v157, v157, s33, v74
	v_med3_f32 v160, v160, s33, v74
	v_med3_f32 v161, v161, s33, v74
	v_cvt_pk_fp8_f32 v103, v188, v191
	v_cvt_pk_fp8_f32 v169, v104, v105
	v_cvt_pk_fp8_f32 v102, v108, v109
	v_cvt_pk_fp8_f32 v171, v112, v113
	v_cvt_pk_fp8_f32 v168, v116, v117
	v_cvt_pk_fp8_f32 v179, v120, v121
	v_cvt_pk_fp8_f32 v178, v124, v125
	v_cvt_pk_fp8_f32 v181, v128, v129
	v_cvt_pk_fp8_f32 v180, v132, v133
	v_cvt_pk_fp8_f32 v183, v136, v137
	v_cvt_pk_fp8_f32 v182, v140, v141
	v_cvt_pk_fp8_f32 v185, v144, v145
	v_cvt_pk_fp8_f32 v184, v148, v149
	v_cvt_pk_fp8_f32 v187, v152, v153
	v_cvt_pk_fp8_f32 v186, v156, v157
	v_cvt_pk_fp8_f32 v189, v160, v161
	v_pk_mul_f32 v[106:107], v[106:107], s[6:7] op_sel_hi:[1,0]
	s_nop 0
	v_med3_f32 v190, v106, s33, v74
	v_med3_f32 v193, v107, s33, v74
	v_pk_mul_f32 v[106:107], v[110:111], s[6:7] op_sel_hi:[1,0]
	v_pk_mul_f32 v[110:111], v[114:115], s[6:7] op_sel_hi:[1,0]
	v_pk_mul_f32 v[114:115], v[118:119], s[6:7] op_sel_hi:[1,0]
	v_pk_mul_f32 v[118:119], v[122:123], s[6:7] op_sel_hi:[1,0]
	v_pk_mul_f32 v[122:123], v[126:127], s[6:7] op_sel_hi:[1,0]
	v_pk_mul_f32 v[126:127], v[130:131], s[6:7] op_sel_hi:[1,0]
	v_pk_mul_f32 v[130:131], v[134:135], s[6:7] op_sel_hi:[1,0]
	v_pk_mul_f32 v[134:135], v[138:139], s[6:7] op_sel_hi:[1,0]
	v_pk_mul_f32 v[138:139], v[142:143], s[6:7] op_sel_hi:[1,0]
	v_pk_mul_f32 v[142:143], v[146:147], s[6:7] op_sel_hi:[1,0]
	v_pk_mul_f32 v[146:147], v[150:151], s[6:7] op_sel_hi:[1,0]
	v_pk_mul_f32 v[150:151], v[154:155], s[6:7] op_sel_hi:[1,0]
	v_pk_mul_f32 v[154:155], v[158:159], s[6:7] op_sel_hi:[1,0]
	v_pk_mul_f32 v[158:159], v[162:163], s[6:7] op_sel_hi:[1,0]
	v_pk_mul_f32 v[162:163], v[166:167], s[6:7] op_sel_hi:[1,0]
	v_med3_f32 v106, v106, s33, v74
	v_med3_f32 v107, v107, s33, v74
	v_med3_f32 v110, v110, s33, v74
	v_med3_f32 v111, v111, s33, v74
	v_med3_f32 v114, v114, s33, v74
	v_med3_f32 v115, v115, s33, v74
	v_med3_f32 v118, v118, s33, v74
	v_med3_f32 v119, v119, s33, v74
	v_med3_f32 v122, v122, s33, v74
	v_med3_f32 v123, v123, s33, v74
	v_med3_f32 v126, v126, s33, v74
	v_med3_f32 v127, v127, s33, v74
	v_med3_f32 v130, v130, s33, v74
	v_med3_f32 v131, v131, s33, v74
	v_med3_f32 v134, v134, s33, v74
	v_med3_f32 v135, v135, s33, v74
	v_med3_f32 v138, v138, s33, v74
	v_med3_f32 v139, v139, s33, v74
	v_med3_f32 v142, v142, s33, v74
	v_med3_f32 v143, v143, s33, v74
	v_med3_f32 v146, v146, s33, v74
	v_med3_f32 v147, v147, s33, v74
	v_med3_f32 v150, v150, s33, v74
	v_med3_f32 v151, v151, s33, v74
	v_med3_f32 v154, v154, s33, v74
	v_med3_f32 v155, v155, s33, v74
	v_med3_f32 v158, v158, s33, v74
	v_med3_f32 v159, v159, s33, v74
	v_med3_f32 v162, v162, s33, v74
	v_med3_f32 v163, v163, s33, v74
	v_cvt_pk_fp8_f32 v103, v190, v193 op_sel:[0,0,1]
	v_cvt_pk_fp8_f32 v169, v106, v107 op_sel:[0,0,1]
	v_cvt_pk_fp8_f32 v102, v110, v111 op_sel:[0,0,1]
	v_cvt_pk_fp8_f32 v171, v114, v115 op_sel:[0,0,1]
	v_cvt_pk_fp8_f32 v168, v118, v119 op_sel:[0,0,1]
	v_cvt_pk_fp8_f32 v179, v122, v123 op_sel:[0,0,1]
	v_cvt_pk_fp8_f32 v178, v126, v127 op_sel:[0,0,1]
	v_cvt_pk_fp8_f32 v181, v130, v131 op_sel:[0,0,1]
	v_cvt_pk_fp8_f32 v180, v134, v135 op_sel:[0,0,1]
	v_cvt_pk_fp8_f32 v183, v138, v139 op_sel:[0,0,1]
	v_cvt_pk_fp8_f32 v182, v142, v143 op_sel:[0,0,1]
	v_cvt_pk_fp8_f32 v185, v146, v147 op_sel:[0,0,1]
	v_cvt_pk_fp8_f32 v184, v150, v151 op_sel:[0,0,1]
	v_cvt_pk_fp8_f32 v187, v154, v155 op_sel:[0,0,1]
	v_cvt_pk_fp8_f32 v186, v158, v159 op_sel:[0,0,1]
	v_cvt_pk_fp8_f32 v189, v162, v163 op_sel:[0,0,1]
	v_perm_b32 v105, v169, v103, s34
	v_perm_b32 v103, v169, v103, s35
	v_perm_b32 v106, v171, v102, s34
	v_perm_b32 v107, v171, v102, s35
	v_perm_b32 v109, v179, v168, s34
	v_perm_b32 v111, v181, v178, s34
	v_perm_b32 v115, v183, v180, s34
	v_perm_b32 v119, v185, v182, s34
	v_perm_b32 v121, v187, v184, s34
	v_perm_b32 v123, v189, v186, s34
	v_perm_b32 v110, v179, v168, s35
	v_perm_b32 v114, v181, v178, s35
	v_perm_b32 v118, v183, v180, s35
	v_perm_b32 v120, v185, v182, s35
	v_perm_b32 v122, v187, v184, s35
	v_perm_b32 v124, v189, v186, s35
	v_perm_b32 v104, v106, v105, s36
	v_perm_b32 v108, v106, v105, s37
	v_perm_b32 v112, v107, v103, s36
	v_perm_b32 v116, v107, v103, s37
	v_perm_b32 v105, v111, v109, s36
	v_perm_b32 v106, v119, v115, s36
	v_perm_b32 v107, v123, v121, s36
	v_perm_b32 v109, v111, v109, s37
	v_perm_b32 v113, v114, v110, s36
	v_perm_b32 v117, v114, v110, s37
	v_perm_b32 v110, v119, v115, s37
	v_perm_b32 v114, v120, v118, s36
	v_perm_b32 v118, v120, v118, s37
	v_perm_b32 v111, v123, v121, s37
	v_perm_b32 v115, v124, v122, s36
	v_perm_b32 v119, v124, v122, s37
	global_store_dwordx4 v[172:173], v[104:107], off nt
	global_store_dwordx4 v[174:175], v[108:111], off nt
	global_store_dwordx4 v[176:177], v[112:115], off nt
	global_store_dwordx4 v[100:101], v[116:119], off nt
	s_lshr_b32 s49, s4, 5
	s_lshl_b32 s50, s49, 11
	v_mov_b32_e32 v101, v69
	v_lshl_or_b32 v100, s49, 6, v1
	s_sub_i32 s49, s47, s50
	s_waitcnt lgkmcnt(1)
; __device__ __forceinline__ void cv_load(const float* W, int N, int nblk, int item, int lane, f32x4 (&tv)[16]) {
;     const int kb = item / nblk, nb = item - kb * nblk; const float* p = W + (size_t)(64 * kb + 16 * (lane >> 4)) * N + 64 * nb + 4 * (lane & 15);
; #pragma unroll
;     for (int i = 0; i < 16; ++i) tv[i] = __builtin_nontemporal_load((const f32x4*)(p + (size_t)i * N));
; }
; template <int MODE> __device__ __forceinline__ void cv_finish(const f32x4 (&tv)[16], int K, int nblk, unsigned char* WT, int item, int lane) {
;     const int kb = item / nblk, nb = item - kb * nblk, k0 = 64 * kb + 16 * (lane >> 4), n0 = 64 * nb + 4 * (lane & 15);
;     unsigned D[16];
; #pragma unroll
;     for (int i = 0; i < 16; ++i) { const f32x2 a = (f32x2){tv[i].x, tv[i].y} * (f32x2){1024.f, 1024.f}, b = (f32x2){tv[i].z, tv[i].w} * (f32x2){1024.f, 1024.f};
;         D[i] = pk4_fp8(a.x, a.y, b.x, b.y); }
	v_subrev_u32_e32 v106, s50, v4
	s_waitcnt lgkmcnt(0)
	v_lshlrev_b64 v[104:105], 13, v[100:101]
	s_add_i32 s50, s48, s49
	v_lshl_add_u64 v[104:105], s[8:9], 0, v[104:105]
	s_ashr_i32 s51, s50, 31
	v_lshl_add_u64 v[104:105], s[50:51], 2, v[104:105]
	v_lshl_add_u64 v[114:115], v[104:105], 0, v[68:69]
	v_add_co_u32_e32 v116, vcc, s17, v114
	v_add_u32_e32 v106, s48, v106
	s_nop 0
	v_addc_co_u32_e32 v117, vcc, 0, v115, vcc
	v_add_co_u32_e32 v118, vcc, s18, v114
	v_ashrrev_i32_e32 v107, 31, v106
	s_nop 0
	v_addc_co_u32_e32 v119, vcc, 0, v115, vcc
	v_add_co_u32_e32 v120, vcc, s19, v114
	v_add_u32_e32 v108, 1, v106
	s_nop 0
	v_addc_co_u32_e32 v121, vcc, 0, v115, vcc
	v_add_co_u32_e32 v122, vcc, s20, v114
	s_waitcnt vmcnt(2)
	v_add_u32_e32 v110, 2, v106
	v_addc_co_u32_e32 v123, vcc, 0, v115, vcc
	v_add_co_u32_e32 v124, vcc, s21, v114
	v_add_u32_e32 v112, 3, v106
	s_nop 0
	v_addc_co_u32_e32 v125, vcc, 0, v115, vcc
	v_add_co_u32_e32 v128, vcc, s22, v114
	v_lshl_add_u64 v[100:101], s[10:11], 0, v[100:101]
	s_nop 0
	v_addc_co_u32_e32 v129, vcc, 0, v115, vcc
	v_add_co_u32_e32 v132, vcc, s23, v114
	v_lshlrev_b64 v[106:107], 11, v[106:107]
	s_nop 0
	v_addc_co_u32_e32 v133, vcc, 0, v115, vcc
	v_add_co_u32_e32 v136, vcc, s24, v114
	v_ashrrev_i32_e32 v109, 31, v108
	s_nop 0
	v_addc_co_u32_e32 v137, vcc, 0, v115, vcc
	v_add_co_u32_e32 v140, vcc, s25, v114
	v_ashrrev_i32_e32 v111, 31, v110
	s_nop 0
	v_addc_co_u32_e32 v141, vcc, 0, v115, vcc
	v_add_co_u32_e32 v144, vcc, s26, v114
	v_ashrrev_i32_e32 v113, 31, v112
	s_nop 0
	v_addc_co_u32_e32 v145, vcc, 0, v115, vcc
	v_add_co_u32_e32 v148, vcc, s27, v114
	v_lshl_add_u64 v[172:173], v[100:101], 0, v[106:107]
	s_nop 0
	v_addc_co_u32_e32 v149, vcc, 0, v115, vcc
	v_add_co_u32_e32 v152, vcc, s28, v114
	v_lshlrev_b64 v[108:109], 11, v[108:109]
	s_nop 0
	v_addc_co_u32_e32 v153, vcc, 0, v115, vcc
	v_add_co_u32_e32 v156, vcc, s29, v114
	v_lshlrev_b64 v[110:111], 11, v[110:111]
	s_nop 0
	v_addc_co_u32_e32 v157, vcc, 0, v115, vcc
	v_add_co_u32_e32 v160, vcc, s30, v114
	v_lshlrev_b64 v[112:113], 11, v[112:113]
	s_nop 0
	v_addc_co_u32_e32 v161, vcc, 0, v115, vcc
	v_add_co_u32_e32 v164, vcc, s31, v114
	global_load_dwordx4 v[104:107], v[114:115], off nt
	s_nop 0
	v_addc_co_u32_e32 v165, vcc, 0, v115, vcc
	v_lshl_add_u64 v[174:175], v[100:101], 0, v[108:109]
	v_lshl_add_u64 v[176:177], v[100:101], 0, v[110:111]
	v_lshl_add_u64 v[100:101], v[100:101], 0, v[112:113]
	global_load_dwordx4 v[108:111], v[116:117], off nt
	global_load_dwordx4 v[112:115], v[118:119], off nt
	s_nop 0
	global_load_dwordx4 v[116:119], v[120:121], off nt
	s_nop 0
	global_load_dwordx4 v[120:123], v[122:123], off nt
	s_nop 0
	global_load_dwordx4 v[124:127], v[124:125], off nt
	s_nop 0
	global_load_dwordx4 v[128:131], v[128:129], off nt
	s_nop 0
	global_load_dwordx4 v[132:135], v[132:133], off nt
	s_nop 0
	global_load_dwordx4 v[136:139], v[136:137], off nt
	s_nop 0
	global_load_dwordx4 v[140:143], v[140:141], off nt
	s_nop 0
	global_load_dwordx4 v[144:147], v[144:145], off nt
	s_nop 0
	global_load_dwordx4 v[148:151], v[148:149], off nt
	s_nop 0
	global_load_dwordx4 v[152:155], v[152:153], off nt
	s_nop 0
	global_load_dwordx4 v[156:159], v[156:157], off nt
	s_nop 0
	global_load_dwordx4 v[160:163], v[160:161], off nt
	s_nop 0
	global_load_dwordx4 v[164:167], v[164:165], off nt
	v_mov_b32_e32 v103, v69
	v_mov_b32_e32 v169, v69
	v_mov_b32_e32 v102, v69
	v_mov_b32_e32 v171, v69
	v_mov_b32_e32 v168, v69
	v_mov_b32_e32 v179, v69
	v_mov_b32_e32 v178, v69
	v_mov_b32_e32 v181, v69
	v_mov_b32_e32 v180, v69
	v_mov_b32_e32 v183, v69
	v_mov_b32_e32 v182, v69
	v_mov_b32_e32 v185, v69
	v_mov_b32_e32 v184, v69
	v_mov_b32_e32 v187, v69
	v_mov_b32_e32 v186, v69
	v_mov_b32_e32 v189, v69
	s_add_i32 s4, s4, 1
	s_add_i32 s48, s48, 64
	s_cmpk_eq_i32 s48, 0x100
	s_waitcnt vmcnt(35)
	v_pk_mul_f32 v[6:7], v[6:7], s[6:7] op_sel_hi:[1,0]
	s_nop 0
	v_med3_f32 v96, v6, s33, v74
	v_med3_f32 v97, v7, s33, v74
	s_waitcnt vmcnt(34)
	v_pk_mul_f32 v[6:7], v[10:11], s[6:7] op_sel_hi:[1,0]
	s_waitcnt vmcnt(33)
	v_pk_mul_f32 v[10:11], v[14:15], s[6:7] op_sel_hi:[1,0]
	s_waitcnt vmcnt(32)
	v_pk_mul_f32 v[14:15], v[18:19], s[6:7] op_sel_hi:[1,0]
	s_waitcnt vmcnt(31)
	v_pk_mul_f32 v[18:19], v[22:23], s[6:7] op_sel_hi:[1,0]
	s_waitcnt vmcnt(30)
	v_pk_mul_f32 v[22:23], v[26:27], s[6:7] op_sel_hi:[1,0]
	s_waitcnt vmcnt(29)
	v_pk_mul_f32 v[26:27], v[30:31], s[6:7] op_sel_hi:[1,0]
	s_waitcnt vmcnt(28)
	v_pk_mul_f32 v[30:31], v[34:35], s[6:7] op_sel_hi:[1,0]
	s_waitcnt vmcnt(27)
	v_pk_mul_f32 v[34:35], v[38:39], s[6:7] op_sel_hi:[1,0]
	s_waitcnt vmcnt(26)
	v_pk_mul_f32 v[38:39], v[42:43], s[6:7] op_sel_hi:[1,0]
	s_waitcnt vmcnt(25)
	v_pk_mul_f32 v[42:43], v[46:47], s[6:7] op_sel_hi:[1,0]
	s_waitcnt vmcnt(24)
	v_pk_mul_f32 v[46:47], v[50:51], s[6:7] op_sel_hi:[1,0]
	s_waitcnt vmcnt(23)
	v_pk_mul_f32 v[50:51], v[54:55], s[6:7] op_sel_hi:[1,0]
	s_waitcnt vmcnt(22)
	v_pk_mul_f32 v[54:55], v[58:59], s[6:7] op_sel_hi:[1,0]
	s_waitcnt vmcnt(21)
	v_pk_mul_f32 v[58:59], v[62:63], s[6:7] op_sel_hi:[1,0]
	s_waitcnt vmcnt(20)
; template <int MODE> __device__ __forceinline__ void cv_finish(const f32x4 (&tv)[16], int K, int nblk, unsigned char* WT, int item, int lane) {
;     const int kb = item / nblk, nb = item - kb * nblk, k0 = 64 * kb + 16 * (lane >> 4), n0 = 64 * nb + 4 * (lane & 15);
;     unsigned D[16];
; #pragma unroll
;     for (int i = 0; i < 16; ++i) { const f32x2 a = (f32x2){tv[i].x, tv[i].y} * (f32x2){1024.f, 1024.f}, b = (f32x2){tv[i].z, tv[i].w} * (f32x2){1024.f, 1024.f};
;         D[i] = pk4_fp8(a.x, a.y, b.x, b.y); }
;     unsigned O[4][4];
; #pragma unroll
;     for (int q = 0; q < 4; ++q) { const unsigned a = D[4 * q], b = D[4 * q + 1], c = D[4 * q + 2], d = D[4 * q + 3];
;         const unsigned t0 = __builtin_amdgcn_perm(b, a, 0x05010400u), t1 = __builtin_amdgcn_perm(b, a, 0x07030602u), u0 = __builtin_amdgcn_perm(d, c, 0x05010400u), u1 = __builtin_amdgcn_perm(d, c, 0x07030602u);
;         O[0][q] = __builtin_amdgcn_perm(u0, t0, 0x05040100u); O[1][q] = __builtin_amdgcn_perm(u0, t0, 0x07060302u); O[2][q] = __builtin_amdgcn_perm(u1, t1, 0x05040100u); O[3][q] = __builtin_amdgcn_perm(u1, t1, 0x07060302u); }
; #pragma unroll
;     for (int j = 0; j < 4; ++j) { u32x4 o; o.x = O[j][0]; o.y = O[j][1]; o.z = O[j][2]; o.w = O[j][3];
;         __builtin_nontemporal_store(o, (u32x4*)(WT + (size_t)drow<MODE>(n0 + j) * K + k0)); }
; }
	v_pk_mul_f32 v[62:63], v[70:71], s[6:7] op_sel_hi:[1,0]
	v_med3_f32 v6, v6, s33, v74
	v_med3_f32 v7, v7, s33, v74
	v_med3_f32 v10, v10, s33, v74
	v_med3_f32 v11, v11, s33, v74
	v_med3_f32 v14, v14, s33, v74
	v_med3_f32 v15, v15, s33, v74
	v_med3_f32 v18, v18, s33, v74
	v_med3_f32 v19, v19, s33, v74
	v_med3_f32 v22, v22, s33, v74
	v_med3_f32 v23, v23, s33, v74
	v_med3_f32 v26, v26, s33, v74
	v_med3_f32 v27, v27, s33, v74
	v_med3_f32 v30, v30, s33, v74
	v_med3_f32 v31, v31, s33, v74
	v_med3_f32 v34, v34, s33, v74
	v_med3_f32 v35, v35, s33, v74
	v_med3_f32 v38, v38, s33, v74
	v_med3_f32 v39, v39, s33, v74
	v_med3_f32 v42, v42, s33, v74
	v_med3_f32 v43, v43, s33, v74
	v_med3_f32 v46, v46, s33, v74
	v_med3_f32 v47, v47, s33, v74
	v_med3_f32 v50, v50, s33, v74
	v_med3_f32 v51, v51, s33, v74
	v_med3_f32 v54, v54, s33, v74
	v_med3_f32 v55, v55, s33, v74
	v_med3_f32 v58, v58, s33, v74
	v_med3_f32 v59, v59, s33, v74
	v_med3_f32 v62, v62, s33, v74
	v_med3_f32 v63, v63, s33, v74
	v_cvt_pk_fp8_f32 v5, v96, v97
	v_cvt_pk_fp8_f32 v75, v6, v7
	v_cvt_pk_fp8_f32 v82, v10, v11
	v_cvt_pk_fp8_f32 v83, v14, v15
	v_cvt_pk_fp8_f32 v84, v18, v19
	v_cvt_pk_fp8_f32 v85, v22, v23
	v_cvt_pk_fp8_f32 v86, v26, v27
	v_cvt_pk_fp8_f32 v87, v30, v31
	v_cvt_pk_fp8_f32 v88, v34, v35
	v_cvt_pk_fp8_f32 v89, v38, v39
	v_cvt_pk_fp8_f32 v90, v42, v43
	v_cvt_pk_fp8_f32 v91, v46, v47
	v_cvt_pk_fp8_f32 v92, v50, v51
	v_cvt_pk_fp8_f32 v93, v54, v55
	v_cvt_pk_fp8_f32 v94, v58, v59
	v_cvt_pk_fp8_f32 v95, v62, v63
	v_pk_mul_f32 v[8:9], v[8:9], s[6:7] op_sel_hi:[1,0]
	s_nop 0
	v_med3_f32 v98, v8, s33, v74
	v_med3_f32 v99, v9, s33, v74
	v_pk_mul_f32 v[8:9], v[12:13], s[6:7] op_sel_hi:[1,0]
	v_pk_mul_f32 v[12:13], v[16:17], s[6:7] op_sel_hi:[1,0]
	v_pk_mul_f32 v[16:17], v[20:21], s[6:7] op_sel_hi:[1,0]
	v_pk_mul_f32 v[20:21], v[24:25], s[6:7] op_sel_hi:[1,0]
	v_pk_mul_f32 v[24:25], v[28:29], s[6:7] op_sel_hi:[1,0]
	v_pk_mul_f32 v[28:29], v[32:33], s[6:7] op_sel_hi:[1,0]
	v_pk_mul_f32 v[32:33], v[36:37], s[6:7] op_sel_hi:[1,0]
	v_pk_mul_f32 v[36:37], v[40:41], s[6:7] op_sel_hi:[1,0]
	v_pk_mul_f32 v[40:41], v[44:45], s[6:7] op_sel_hi:[1,0]
	v_pk_mul_f32 v[44:45], v[48:49], s[6:7] op_sel_hi:[1,0]
	v_pk_mul_f32 v[48:49], v[52:53], s[6:7] op_sel_hi:[1,0]
	v_pk_mul_f32 v[52:53], v[56:57], s[6:7] op_sel_hi:[1,0]
	v_pk_mul_f32 v[56:57], v[60:61], s[6:7] op_sel_hi:[1,0]
	v_pk_mul_f32 v[60:61], v[64:65], s[6:7] op_sel_hi:[1,0]
	v_pk_mul_f32 v[64:65], v[72:73], s[6:7] op_sel_hi:[1,0]
	v_med3_f32 v8, v8, s33, v74
	v_med3_f32 v9, v9, s33, v74
	v_med3_f32 v12, v12, s33, v74
	v_med3_f32 v13, v13, s33, v74
	v_med3_f32 v16, v16, s33, v74
	v_med3_f32 v17, v17, s33, v74
	v_med3_f32 v20, v20, s33, v74
	v_med3_f32 v21, v21, s33, v74
	v_med3_f32 v24, v24, s33, v74
	v_med3_f32 v25, v25, s33, v74
	v_med3_f32 v28, v28, s33, v74
	v_med3_f32 v29, v29, s33, v74
	v_med3_f32 v32, v32, s33, v74
	v_med3_f32 v33, v33, s33, v74
	v_med3_f32 v36, v36, s33, v74
	v_med3_f32 v37, v37, s33, v74
	v_med3_f32 v40, v40, s33, v74
	v_med3_f32 v41, v41, s33, v74
	v_med3_f32 v44, v44, s33, v74
	v_med3_f32 v45, v45, s33, v74
	v_med3_f32 v48, v48, s33, v74
	v_med3_f32 v49, v49, s33, v74
	v_med3_f32 v52, v52, s33, v74
	v_med3_f32 v53, v53, s33, v74
	v_med3_f32 v56, v56, s33, v74
	v_med3_f32 v57, v57, s33, v74
	v_med3_f32 v60, v60, s33, v74
	v_med3_f32 v61, v61, s33, v74
	v_med3_f32 v64, v64, s33, v74
	v_med3_f32 v65, v65, s33, v74
	v_cvt_pk_fp8_f32 v5, v98, v99 op_sel:[0,0,1]
	v_cvt_pk_fp8_f32 v75, v8, v9 op_sel:[0,0,1]
	v_cvt_pk_fp8_f32 v82, v12, v13 op_sel:[0,0,1]
	v_cvt_pk_fp8_f32 v83, v16, v17 op_sel:[0,0,1]
	v_cvt_pk_fp8_f32 v84, v20, v21 op_sel:[0,0,1]
	v_cvt_pk_fp8_f32 v85, v24, v25 op_sel:[0,0,1]
	v_cvt_pk_fp8_f32 v86, v28, v29 op_sel:[0,0,1]
	v_cvt_pk_fp8_f32 v87, v32, v33 op_sel:[0,0,1]
	v_cvt_pk_fp8_f32 v88, v36, v37 op_sel:[0,0,1]
	v_cvt_pk_fp8_f32 v89, v40, v41 op_sel:[0,0,1]
	v_cvt_pk_fp8_f32 v90, v44, v45 op_sel:[0,0,1]
	v_cvt_pk_fp8_f32 v91, v48, v49 op_sel:[0,0,1]
	v_cvt_pk_fp8_f32 v92, v52, v53 op_sel:[0,0,1]
	v_cvt_pk_fp8_f32 v93, v56, v57 op_sel:[0,0,1]
	v_cvt_pk_fp8_f32 v94, v60, v61 op_sel:[0,0,1]
	v_cvt_pk_fp8_f32 v95, v64, v65 op_sel:[0,0,1]
	v_perm_b32 v7, v75, v5, s34
	v_perm_b32 v5, v75, v5, s35
	v_perm_b32 v8, v83, v82, s34
	v_perm_b32 v9, v83, v82, s35
	v_perm_b32 v11, v85, v84, s34
	v_perm_b32 v13, v87, v86, s34
	v_perm_b32 v17, v89, v88, s34
	v_perm_b32 v21, v91, v90, s34
	v_perm_b32 v23, v93, v92, s34
	v_perm_b32 v25, v95, v94, s34
	v_perm_b32 v12, v85, v84, s35
	v_perm_b32 v16, v87, v86, s35
	v_perm_b32 v20, v89, v88, s35
	v_perm_b32 v22, v91, v90, s35
	v_perm_b32 v24, v93, v92, s35
	v_perm_b32 v26, v95, v94, s35
	v_perm_b32 v6, v8, v7, s36
	v_perm_b32 v10, v8, v7, s37
	v_perm_b32 v14, v9, v5, s36
	v_perm_b32 v18, v9, v5, s37
	v_perm_b32 v7, v13, v11, s36
	v_perm_b32 v8, v21, v17, s36
	v_perm_b32 v9, v25, v23, s36
	v_perm_b32 v11, v13, v11, s37
	v_perm_b32 v15, v16, v12, s36
	v_perm_b32 v19, v16, v12, s37
	v_perm_b32 v12, v21, v17, s37
	v_perm_b32 v16, v22, v20, s36
	v_perm_b32 v20, v22, v20, s37
	v_perm_b32 v13, v25, v23, s37
	v_perm_b32 v17, v26, v24, s36
	v_perm_b32 v21, v26, v24, s37
	global_store_dwordx4 v[76:77], v[6:9], off nt
	global_store_dwordx4 v[78:79], v[10:13], off nt
	global_store_dwordx4 v[80:81], v[14:17], off nt
	global_store_dwordx4 v[2:3], v[18:21], off nt
	s_waitcnt vmcnt(19)
	v_pk_mul_f32 v[104:105], v[104:105], s[6:7] op_sel_hi:[1,0]
	s_nop 0
	v_med3_f32 v188, v104, s33, v74
	v_med3_f32 v191, v105, s33, v74
	s_waitcnt vmcnt(18)
	v_pk_mul_f32 v[104:105], v[108:109], s[6:7] op_sel_hi:[1,0]
	s_waitcnt vmcnt(17)
	v_pk_mul_f32 v[108:109], v[112:113], s[6:7] op_sel_hi:[1,0]
	s_waitcnt vmcnt(16)
; template <int MODE> __device__ __forceinline__ void cv_finish(const f32x4 (&tv)[16], int K, int nblk, unsigned char* WT, int item, int lane) {
;     const int kb = item / nblk, nb = item - kb * nblk, k0 = 64 * kb + 16 * (lane >> 4), n0 = 64 * nb + 4 * (lane & 15);
;     unsigned D[16];
; #pragma unroll
;     for (int i = 0; i < 16; ++i) { const f32x2 a = (f32x2){tv[i].x, tv[i].y} * (f32x2){1024.f, 1024.f}, b = (f32x2){tv[i].z, tv[i].w} * (f32x2){1024.f, 1024.f};
;         D[i] = pk4_fp8(a.x, a.y, b.x, b.y); }
;     unsigned O[4][4];
; #pragma unroll
;     for (int q = 0; q < 4; ++q) { const unsigned a = D[4 * q], b = D[4 * q + 1], c = D[4 * q + 2], d = D[4 * q + 3];
;         const unsigned t0 = __builtin_amdgcn_perm(b, a, 0x05010400u), t1 = __builtin_amdgcn_perm(b, a, 0x07030602u), u0 = __builtin_amdgcn_perm(d, c, 0x05010400u), u1 = __builtin_amdgcn_perm(d, c, 0x07030602u);
;         O[0][q] = __builtin_amdgcn_perm(u0, t0, 0x05040100u); O[1][q] = __builtin_amdgcn_perm(u0, t0, 0x07060302u); O[2][q] = __builtin_amdgcn_perm(u1, t1, 0x05040100u); O[3][q] = __builtin_amdgcn_perm(u1, t1, 0x07060302u); }
; #pragma unroll
;     for (int j = 0; j < 4; ++j) { u32x4 o; o.x = O[j][0]; o.y = O[j][1]; o.z = O[j][2]; o.w = O[j][3];
;         __builtin_nontemporal_store(o, (u32x4*)(WT + (size_t)drow<MODE>(n0 + j) * K + k0)); }
; }
; template <int MODE> __device__ __forceinline__ void cv_run4(const float* W, int K, int N, unsigned char* WT, int item0, int lane) {
;     const int nblk = N / 64; f32x4 ta[16];
; #pragma unroll 1
;     for (int j = 0; j < 4; ++j) { cv_load(W, N, nblk, item0 + j, lane, ta); cv_finish<MODE>(ta, K, nblk, WT, item0 + j, lane); }
	v_pk_mul_f32 v[112:113], v[116:117], s[6:7] op_sel_hi:[1,0]
	s_waitcnt vmcnt(15)
	v_pk_mul_f32 v[116:117], v[120:121], s[6:7] op_sel_hi:[1,0]
	s_waitcnt vmcnt(14)
	v_pk_mul_f32 v[120:121], v[124:125], s[6:7] op_sel_hi:[1,0]
	s_waitcnt vmcnt(13)
	v_pk_mul_f32 v[124:125], v[128:129], s[6:7] op_sel_hi:[1,0]
	s_waitcnt vmcnt(12)
	v_pk_mul_f32 v[128:129], v[132:133], s[6:7] op_sel_hi:[1,0]
	s_waitcnt vmcnt(11)
	v_pk_mul_f32 v[132:133], v[136:137], s[6:7] op_sel_hi:[1,0]
	s_waitcnt vmcnt(10)
	v_pk_mul_f32 v[136:137], v[140:141], s[6:7] op_sel_hi:[1,0]
	s_waitcnt vmcnt(9)
	v_pk_mul_f32 v[140:141], v[144:145], s[6:7] op_sel_hi:[1,0]
	s_waitcnt vmcnt(8)
	v_pk_mul_f32 v[144:145], v[148:149], s[6:7] op_sel_hi:[1,0]
	s_waitcnt vmcnt(7)
	v_pk_mul_f32 v[148:149], v[152:153], s[6:7] op_sel_hi:[1,0]
	s_waitcnt vmcnt(6)
	v_pk_mul_f32 v[152:153], v[156:157], s[6:7] op_sel_hi:[1,0]
	s_waitcnt vmcnt(5)
	v_pk_mul_f32 v[156:157], v[160:161], s[6:7] op_sel_hi:[1,0]
	s_waitcnt vmcnt(4)
	v_pk_mul_f32 v[160:161], v[164:165], s[6:7] op_sel_hi:[1,0]
	v_med3_f32 v104, v104, s33, v74
	v_med3_f32 v105, v105, s33, v74
	v_med3_f32 v108, v108, s33, v74
	v_med3_f32 v109, v109, s33, v74
	v_med3_f32 v112, v112, s33, v74
	v_med3_f32 v113, v113, s33, v74
	v_med3_f32 v116, v116, s33, v74
	v_med3_f32 v117, v117, s33, v74
	v_med3_f32 v120, v120, s33, v74
	v_med3_f32 v121, v121, s33, v74
	v_med3_f32 v124, v124, s33, v74
	v_med3_f32 v125, v125, s33, v74
	v_med3_f32 v128, v128, s33, v74
	v_med3_f32 v129, v129, s33, v74
	v_med3_f32 v132, v132, s33, v74
	v_med3_f32 v133, v133, s33, v74
	v_med3_f32 v136, v136, s33, v74
	v_med3_f32 v137, v137, s33, v74
	v_med3_f32 v140, v140, s33, v74
	v_med3_f32 v141, v141, s33, v74
	v_med3_f32 v144, v144, s33, v74
	v_med3_f32 v145, v145, s33, v74
	v_med3_f32 v148, v148, s33, v74
	v_med3_f32 v149, v149, s33, v74
	v_med3_f32 v152, v152, s33, v74
	v_med3_f32 v153, v153, s33, v74
	v_med3_f32 v156, v156, s33, v74
	v_med3_f32 v157, v157, s33, v74
	v_med3_f32 v160, v160, s33, v74
	v_med3_f32 v161, v161, s33, v74
	v_cvt_pk_fp8_f32 v103, v188, v191
	v_cvt_pk_fp8_f32 v169, v104, v105
	v_cvt_pk_fp8_f32 v102, v108, v109
	v_cvt_pk_fp8_f32 v171, v112, v113
	v_cvt_pk_fp8_f32 v168, v116, v117
	v_cvt_pk_fp8_f32 v179, v120, v121
	v_cvt_pk_fp8_f32 v178, v124, v125
	v_cvt_pk_fp8_f32 v181, v128, v129
	v_cvt_pk_fp8_f32 v180, v132, v133
	v_cvt_pk_fp8_f32 v183, v136, v137
	v_cvt_pk_fp8_f32 v182, v140, v141
	v_cvt_pk_fp8_f32 v185, v144, v145
	v_cvt_pk_fp8_f32 v184, v148, v149
	v_cvt_pk_fp8_f32 v187, v152, v153
	v_cvt_pk_fp8_f32 v186, v156, v157
	v_cvt_pk_fp8_f32 v189, v160, v161
	v_pk_mul_f32 v[106:107], v[106:107], s[6:7] op_sel_hi:[1,0]
	s_nop 0
	v_med3_f32 v190, v106, s33, v74
	v_med3_f32 v193, v107, s33, v74
	v_pk_mul_f32 v[106:107], v[110:111], s[6:7] op_sel_hi:[1,0]
	v_pk_mul_f32 v[110:111], v[114:115], s[6:7] op_sel_hi:[1,0]
	v_pk_mul_f32 v[114:115], v[118:119], s[6:7] op_sel_hi:[1,0]
	v_pk_mul_f32 v[118:119], v[122:123], s[6:7] op_sel_hi:[1,0]
	v_pk_mul_f32 v[122:123], v[126:127], s[6:7] op_sel_hi:[1,0]
	v_pk_mul_f32 v[126:127], v[130:131], s[6:7] op_sel_hi:[1,0]
	v_pk_mul_f32 v[130:131], v[134:135], s[6:7] op_sel_hi:[1,0]
	v_pk_mul_f32 v[134:135], v[138:139], s[6:7] op_sel_hi:[1,0]
	v_pk_mul_f32 v[138:139], v[142:143], s[6:7] op_sel_hi:[1,0]
	v_pk_mul_f32 v[142:143], v[146:147], s[6:7] op_sel_hi:[1,0]
	v_pk_mul_f32 v[146:147], v[150:151], s[6:7] op_sel_hi:[1,0]
	v_pk_mul_f32 v[150:151], v[154:155], s[6:7] op_sel_hi:[1,0]
	v_pk_mul_f32 v[154:155], v[158:159], s[6:7] op_sel_hi:[1,0]
	v_pk_mul_f32 v[158:159], v[162:163], s[6:7] op_sel_hi:[1,0]
	v_pk_mul_f32 v[162:163], v[166:167], s[6:7] op_sel_hi:[1,0]
	v_med3_f32 v106, v106, s33, v74
	v_med3_f32 v107, v107, s33, v74
	v_med3_f32 v110, v110, s33, v74
	v_med3_f32 v111, v111, s33, v74
	v_med3_f32 v114, v114, s33, v74
	v_med3_f32 v115, v115, s33, v74
	v_med3_f32 v118, v118, s33, v74
	v_med3_f32 v119, v119, s33, v74
	v_med3_f32 v122, v122, s33, v74
	v_med3_f32 v123, v123, s33, v74
	v_med3_f32 v126, v126, s33, v74
	v_med3_f32 v127, v127, s33, v74
	v_med3_f32 v130, v130, s33, v74
	v_med3_f32 v131, v131, s33, v74
	v_med3_f32 v134, v134, s33, v74
	v_med3_f32 v135, v135, s33, v74
	v_med3_f32 v138, v138, s33, v74
	v_med3_f32 v139, v139, s33, v74
	v_med3_f32 v142, v142, s33, v74
	v_med3_f32 v143, v143, s33, v74
	v_med3_f32 v146, v146, s33, v74
	v_med3_f32 v147, v147, s33, v74
	v_med3_f32 v150, v150, s33, v74
	v_med3_f32 v151, v151, s33, v74
	v_med3_f32 v154, v154, s33, v74
	v_med3_f32 v155, v155, s33, v74
	v_med3_f32 v158, v158, s33, v74
	v_med3_f32 v159, v159, s33, v74
	v_med3_f32 v162, v162, s33, v74
	v_med3_f32 v163, v163, s33, v74
	v_cvt_pk_fp8_f32 v103, v190, v193 op_sel:[0,0,1]
	v_cvt_pk_fp8_f32 v169, v106, v107 op_sel:[0,0,1]
	v_cvt_pk_fp8_f32 v102, v110, v111 op_sel:[0,0,1]
	v_cvt_pk_fp8_f32 v171, v114, v115 op_sel:[0,0,1]
	v_cvt_pk_fp8_f32 v168, v118, v119 op_sel:[0,0,1]
	v_cvt_pk_fp8_f32 v179, v122, v123 op_sel:[0,0,1]
	v_cvt_pk_fp8_f32 v178, v126, v127 op_sel:[0,0,1]
	v_cvt_pk_fp8_f32 v181, v130, v131 op_sel:[0,0,1]
	v_cvt_pk_fp8_f32 v180, v134, v135 op_sel:[0,0,1]
	v_cvt_pk_fp8_f32 v183, v138, v139 op_sel:[0,0,1]
	v_cvt_pk_fp8_f32 v182, v142, v143 op_sel:[0,0,1]
	v_cvt_pk_fp8_f32 v185, v146, v147 op_sel:[0,0,1]
	v_cvt_pk_fp8_f32 v184, v150, v151 op_sel:[0,0,1]
	v_cvt_pk_fp8_f32 v187, v154, v155 op_sel:[0,0,1]
	v_cvt_pk_fp8_f32 v186, v158, v159 op_sel:[0,0,1]
	v_cvt_pk_fp8_f32 v189, v162, v163 op_sel:[0,0,1]
	v_perm_b32 v105, v169, v103, s34
	v_perm_b32 v103, v169, v103, s35
	v_perm_b32 v106, v171, v102, s34
	v_perm_b32 v107, v171, v102, s35
	v_perm_b32 v109, v179, v168, s34
	v_perm_b32 v111, v181, v178, s34
	v_perm_b32 v115, v183, v180, s34
	v_perm_b32 v119, v185, v182, s34
	v_perm_b32 v121, v187, v184, s34
	v_perm_b32 v123, v189, v186, s34
	v_perm_b32 v110, v179, v168, s35
	v_perm_b32 v114, v181, v178, s35
	v_perm_b32 v118, v183, v180, s35
	v_perm_b32 v120, v185, v182, s35
	v_perm_b32 v122, v187, v184, s35
	v_perm_b32 v124, v189, v186, s35
	v_perm_b32 v104, v106, v105, s36
	v_perm_b32 v108, v106, v105, s37
	v_perm_b32 v112, v107, v103, s36
	v_perm_b32 v116, v107, v103, s37
	v_perm_b32 v105, v111, v109, s36
	v_perm_b32 v106, v119, v115, s36
	v_perm_b32 v107, v123, v121, s36
	v_perm_b32 v109, v111, v109, s37
	v_perm_b32 v113, v114, v110, s36
	v_perm_b32 v117, v114, v110, s37
	v_perm_b32 v110, v119, v115, s37
	v_perm_b32 v114, v120, v118, s36
	v_perm_b32 v118, v120, v118, s37
	v_perm_b32 v111, v123, v121, s37
	v_perm_b32 v115, v124, v122, s36
	v_perm_b32 v119, v124, v122, s37
	global_store_dwordx4 v[172:173], v[104:107], off nt
	global_store_dwordx4 v[174:175], v[108:111], off nt
	global_store_dwordx4 v[176:177], v[112:115], off nt
	global_store_dwordx4 v[100:101], v[116:119], off nt
	s_cbranch_scc0 .LBB0_979
	s_mov_b64 s[8:9], 0
